# final combine phases: nt on the read-once routing index/weight loads (on the full stack)
# speedup vs baseline: 1.0013x; 1.0013x over previous
; #define LAS __attribute__((address_space(3)))
; __device__ __forceinline__ void moe_tables_load(const Args& a, const Frame& F) {
;     LAS int* pst = (LAS int*)(F.misc + LM_PSTART); LAS unsigned char* tg = F.misc + LM_TILEG; LAS int* cxs = (LAS int*)(F.misc + LM_CX);
;     const int* tab = (const int*)(a.ws + WS_MOETAB);
;     __syncthreads();
;     if (F.tid < 65) pst[F.tid] = tab[F.tid];
;     if (F.tid == 65) cxs[0] = tab[65];
;     if (F.tid >= 128 && F.tid < 128 + 288) ((LAS int*)tg)[F.tid - 128] = tab[128 + F.tid - 128];
;     __syncthreads();
; }
; __device__ __forceinline__ void p_final(const Args& a, const Frame& F, int half) {
;     moe_tables_load(a, F);
.LBB0_1230:
	s_cmp_lt_i32 s74, 14
	s_cselect_b64 s[4:5], -1, 0
	s_and_b64 s[0:1], s[4:5], s[0:1]
	s_andn2_b64 vcc, exec, s[0:1]
	s_cbranch_vccnz .LBB0_1242
	s_add_u32 s4, s72, 0xa80000
	s_movk_i32 s8, 0x41
	s_addc_u32 s5, s73, 0
	v_cmp_gt_u32_e32 vcc, s8, v0
	s_waitcnt vmcnt(0) lgkmcnt(0)
	s_barrier
	s_and_saveexec_b64 s[6:7], vcc
	s_cbranch_execz .LBB0_1233
	v_lshlrev_b32_e32 v1, 2, v0
	global_load_dword v2, v1, s[4:5] nt
	v_add_u32_e32 v1, 0, v1
	v_add_u32_e32 v1, 0x22200, v1
	s_waitcnt vmcnt(0)
	ds_write_b32 v1, v2

; #define LAS __attribute__((address_space(3)))
; __device__ __forceinline__ void moe_tables_load(const Args& a, const Frame& F) {
;     ...
;     if (F.tid >= 128 && F.tid < 128 + 288) ((LAS int*)tg)[F.tid - 128] = tab[128 + F.tid - 128];
.LBB0_1235:
	s_or_b64 exec, exec, s[6:7]
	v_add_u32_e32 v1, 0xffffff80, v0
	s_movk_i32 s6, 0x120
	v_cmp_gt_u32_e32 vcc, s6, v1
	s_and_saveexec_b64 s[6:7], vcc
	s_cbranch_execz .LBB0_1237
	v_lshlrev_b32_e32 v1, 2, v0
	global_load_dword v2, v1, s[4:5] nt
	v_add_u32_e32 v1, 0, v1
	v_add_u32_e32 v1, 0x22200, v1
	s_waitcnt vmcnt(0)
	ds_write_b32 v1, v2

; __device__ __forceinline__ void p_final(const Args& a, const Frame& F, int half) {
;     ...
;     for (int t = tbeg + gw; t < tend; t += NGW) {
;         f32x4* xr = (f32x4*)(a.out + (size_t)t * D) + F.lane;
;         const u32x2* x1p = (const u32x2*)x1_row(a.out, a.ws, t) + F.lane;
;         const f32x4* g2 = (const f32x4*)(mod + (t >> 13) * 6144 + 5120) + F.lane;
;         int rk[4]; float wk[4];
; #pragma unroll
;         for (int k = 0; k < 4; ++k) { rk[k] = rkn[k]; wk[k] = wkn[k]; }
;         u32x2 ok[4][4], xw[4];
; #pragma unroll
;         for (int j = 0; j < 4; ++j) { xw[j] = x1p[64 * j];
; #pragma unroll
;             for (int k = 0; k < 4; ++k) ok[j][k] = *((const u32x2*)(OUTK + (size_t)rk[k] * D) + F.lane + 64 * j); }
;         { const int tn = t + NGW; if (tn < tend) {
; #pragma unroll
;             for (int k = 0; k < 4; ++k) { rkn[k] = tok_row[tn * 4 + k] - rowbase; wkn[k] = ent_w[tn * 4 + k]; } } }
.LBB0_1240:
	s_add_i32 s9, s4, 0xffff8800
	s_cmpk_lt_i32 s4, 0x7800
	s_cselect_b32 s27, s5, 0
	s_cselect_b32 s26, s4, s9
	s_waitcnt vmcnt(4)
	v_ashrrev_i32_e32 v23, 31, v4
	v_mov_b32_e32 v22, v4
	s_cselect_b32 s9, s22, s20
	s_cselect_b32 s28, s21, s19
	s_lshl_b64 s[26:27], s[26:27], 11
	v_lshlrev_b64 v[22:23], 11, v[22:23]
	s_add_u32 s26, s28, s26
	v_ashrrev_i32_e32 v19, 31, v2
	v_mov_b32_e32 v18, v2
	v_ashrrev_i32_e32 v21, 31, v3
	v_mov_b32_e32 v20, v3
	v_lshl_add_u64 v[70:71], v[14:15], 0, v[22:23]
	v_ashrrev_i32_e32 v23, 31, v5
	v_mov_b32_e32 v22, v5
	s_addc_u32 s27, s9, s27
	v_lshlrev_b64 v[18:19], 11, v[18:19]
	v_lshlrev_b64 v[20:21], 11, v[20:21]
	v_lshlrev_b64 v[22:23], 11, v[22:23]
	v_lshl_add_u64 v[18:19], v[14:15], 0, v[18:19]
	v_lshl_add_u64 v[20:21], v[14:15], 0, v[20:21]
	v_lshl_add_u64 v[72:73], v[14:15], 0, v[22:23]
	global_load_dwordx2 v[52:53], v67, s[26:27] nt
	global_load_dwordx2 v[42:43], v67, s[26:27] offset:512 nt
	global_load_dwordx2 v[32:33], v67, s[26:27] offset:1024 nt
	global_load_dwordx2 v[22:23], v67, s[26:27] offset:1536 nt
	global_load_dwordx2 v[54:55], v[18:19], off nt
	global_load_dwordx2 v[44:45], v[18:19], off offset:512 nt
	global_load_dwordx2 v[34:35], v[18:19], off offset:1024 nt
	global_load_dwordx2 v[28:29], v[18:19], off offset:1536 nt
	global_load_dwordx2 v[56:57], v[20:21], off nt
	global_load_dwordx2 v[46:47], v[20:21], off offset:512 nt
	global_load_dwordx2 v[36:37], v[20:21], off offset:1024 nt
	global_load_dwordx2 v[30:31], v[20:21], off offset:1536 nt
	global_load_dwordx2 v[58:59], v[70:71], off nt
	global_load_dwordx2 v[48:49], v[70:71], off offset:512 nt
	global_load_dwordx2 v[38:39], v[70:71], off offset:1024 nt
	global_load_dwordx2 v[24:25], v[70:71], off offset:1536 nt
	global_load_dwordx2 v[60:61], v[72:73], off nt
	global_load_dwordx2 v[50:51], v[72:73], off offset:512 nt
	global_load_dwordx2 v[40:41], v[72:73], off offset:1024 nt
	global_load_dwordx2 v[26:27], v[72:73], off offset:1536 nt
	s_add_i32 s9, s6, s4
	s_cmp_ge_i32 s9, s14
	s_waitcnt vmcnt(24)
	v_mov_b64_e32 v[20:21], v[6:7]
	v_mov_b64_e32 v[18:19], v[8:9]
	s_cbranch_scc1 .LBB0_1239
	s_add_i32 s26, s8, -3
	s_ashr_i32 s27, s26, 31
	s_lshl_b64 s[26:27], s[26:27], 2
	s_add_u32 s28, s15, s26
	s_addc_u32 s29, s16, s27
	s_add_u32 s26, s17, s26
	s_addc_u32 s27, s18, s27
	s_add_i32 s34, s8, -2
	s_ashr_i32 s35, s34, 31
	s_lshl_b64 s[34:35], s[34:35], 2
	s_add_u32 s36, s15, s34
	s_addc_u32 s37, s16, s35
	s_add_u32 s34, s17, s34
	s_addc_u32 s35, s18, s35
	s_add_i32 s38, s8, -1
	s_ashr_i32 s39, s38, 31
	s_lshl_b64 s[38:39], s[38:39], 2
	s_add_u32 s40, s15, s38
	s_addc_u32 s41, s16, s39
	s_add_u32 s38, s17, s38
	s_addc_u32 s39, s18, s39
	s_ashr_i32 s9, s8, 31
	s_lshl_b64 s[42:43], s[8:9], 2
	s_add_u32 s44, s15, s42
	s_addc_u32 s45, s16, s43
	s_add_u32 s42, s17, s42
	s_addc_u32 s43, s18, s43
	global_load_dword v2, v11, s[28:29] nt
	global_load_dword v20, v11, s[26:27] nt
	global_load_dword v3, v11, s[36:37] nt
	global_load_dword v21, v11, s[34:35] nt
	global_load_dword v4, v11, s[40:41] nt
	global_load_dword v18, v11, s[38:39] nt
	global_load_dword v5, v11, s[44:45] nt
	global_load_dword v19, v11, s[42:43] nt
	s_branch .LBB0_1239

; #define LAS __attribute__((address_space(3)))
; __device__ __forceinline__ void moe_tables_load(const Args& a, const Frame& F) {
;     LAS int* pst = (LAS int*)(F.misc + LM_PSTART); LAS unsigned char* tg = F.misc + LM_TILEG; LAS int* cxs = (LAS int*)(F.misc + LM_CX);
;     const int* tab = (const int*)(a.ws + WS_MOETAB);
;     __syncthreads();
;     if (F.tid < 65) pst[F.tid] = tab[F.tid];
;     if (F.tid == 65) cxs[0] = tab[65];
;     if (F.tid >= 128 && F.tid < 128 + 288) ((LAS int*)tg)[F.tid - 128] = tab[128 + F.tid - 128];
;     __syncthreads();
; }
; __device__ __forceinline__ void p_final(const Args& a, const Frame& F, int half) {
;     moe_tables_load(a, F);
.LBB0_1386:
	s_cmp_lt_i32 s74, 16
	s_cselect_b64 s[4:5], -1, 0
	s_and_b64 s[0:1], s[4:5], s[0:1]
	s_andn2_b64 vcc, exec, s[0:1]
	s_cbranch_vccnz .LBB0_1398
	s_add_u32 s0, s72, 0xa80000
	s_movk_i32 s6, 0x41
	s_addc_u32 s1, s73, 0
	v_cmp_gt_u32_e32 vcc, s6, v0
	v_lshlrev_b32_e32 v1, 2, v0
	s_waitcnt vmcnt(0) lgkmcnt(0)
	s_barrier
	s_and_saveexec_b64 s[4:5], vcc
	s_cbranch_execz .LBB0_1389
	global_load_dword v2, v1, s[0:1] nt
	v_add_u32_e32 v3, 0, v1
	v_add_u32_e32 v3, 0x22200, v3
	s_waitcnt vmcnt(0)
	ds_write_b32 v3, v2

; #define LAS __attribute__((address_space(3)))
; __device__ __forceinline__ void moe_tables_load(const Args& a, const Frame& F) {
;     ...
;     if (F.tid >= 128 && F.tid < 128 + 288) ((LAS int*)tg)[F.tid - 128] = tab[128 + F.tid - 128];
.LBB0_1391:
	s_or_b64 exec, exec, s[4:5]
	v_add_u32_e32 v0, 0xffffff80, v0
	s_movk_i32 s4, 0x120
	v_cmp_gt_u32_e32 vcc, s4, v0
	s_and_saveexec_b64 s[4:5], vcc
	s_cbranch_execz .LBB0_1393
	global_load_dword v0, v1, s[0:1] nt
	v_add_u32_e32 v1, 0, v1
	v_add_u32_e32 v1, 0x22200, v1
	s_waitcnt vmcnt(0)
	ds_write_b32 v1, v0

; __device__ __forceinline__ void p_final(const Args& a, const Frame& F, int half) {
;     ...
;     for (int t = tbeg + gw; t < tend; t += NGW) {
;         f32x4* xr = (f32x4*)(a.out + (size_t)t * D) + F.lane;
;         const u32x2* x1p = (const u32x2*)x1_row(a.out, a.ws, t) + F.lane;
;         const f32x4* g2 = (const f32x4*)(mod + (t >> 13) * 6144 + 5120) + F.lane;
;         int rk[4]; float wk[4];
; #pragma unroll
;         for (int k = 0; k < 4; ++k) { rk[k] = rkn[k]; wk[k] = wkn[k]; }
;         u32x2 ok[4][4], xw[4];
; #pragma unroll
;         for (int j = 0; j < 4; ++j) { xw[j] = x1p[64 * j];
; #pragma unroll
;             for (int k = 0; k < 4; ++k) ok[j][k] = *((const u32x2*)(OUTK + (size_t)rk[k] * D) + F.lane + 64 * j); }
;         { const int tn = t + NGW; if (tn < tend) {
; #pragma unroll
;             for (int k = 0; k < 4; ++k) { rkn[k] = tok_row[tn * 4 + k] - rowbase; wkn[k] = ent_w[tn * 4 + k]; } } }
.LBB0_1396:
	s_add_i32 s7, s0, 0xffff8800
	s_cmpk_lt_i32 s0, 0x7800
	s_cselect_b32 s23, s1, 0
	s_cselect_b32 s22, s0, s7
	v_ashrrev_i32_e32 v21, 31, v14
	v_mov_b32_e32 v20, v14
	s_cselect_b32 s7, s18, s16
	s_cselect_b32 s21, s17, s15
	s_lshl_b64 s[22:23], s[22:23], 11
	v_lshlrev_b64 v[20:21], 11, v[20:21]
	s_add_u32 s22, s21, s22
	v_ashrrev_i32_e32 v17, 31, v12
	v_mov_b32_e32 v16, v12
	v_ashrrev_i32_e32 v19, 31, v13
	v_mov_b32_e32 v18, v13
	v_lshl_add_u64 v[70:71], v[8:9], 0, v[20:21]
	v_ashrrev_i32_e32 v21, 31, v15
	v_mov_b32_e32 v20, v15
	s_addc_u32 s23, s7, s23
	v_lshlrev_b64 v[16:17], 11, v[16:17]
	v_lshlrev_b64 v[18:19], 11, v[18:19]
	v_lshlrev_b64 v[20:21], 11, v[20:21]
	v_lshl_add_u64 v[16:17], v[8:9], 0, v[16:17]
	v_lshl_add_u64 v[18:19], v[8:9], 0, v[18:19]
	v_lshl_add_u64 v[72:73], v[8:9], 0, v[20:21]
	global_load_dwordx2 v[50:51], v60, s[22:23] nt
	global_load_dwordx2 v[40:41], v60, s[22:23] offset:512 nt
	global_load_dwordx2 v[30:31], v60, s[22:23] offset:1024 nt
	global_load_dwordx2 v[20:21], v60, s[22:23] offset:1536 nt
	global_load_dwordx2 v[52:53], v[16:17], off nt
	global_load_dwordx2 v[42:43], v[16:17], off offset:512 nt
	global_load_dwordx2 v[32:33], v[16:17], off offset:1024 nt
	global_load_dwordx2 v[26:27], v[16:17], off offset:1536 nt
	global_load_dwordx2 v[54:55], v[18:19], off nt
	global_load_dwordx2 v[44:45], v[18:19], off offset:512 nt
	global_load_dwordx2 v[34:35], v[18:19], off offset:1024 nt
	global_load_dwordx2 v[28:29], v[18:19], off offset:1536 nt
	global_load_dwordx2 v[56:57], v[70:71], off nt
	global_load_dwordx2 v[46:47], v[70:71], off offset:512 nt
	global_load_dwordx2 v[36:37], v[70:71], off offset:1024 nt
	global_load_dwordx2 v[22:23], v[70:71], off offset:1536 nt
	global_load_dwordx2 v[58:59], v[72:73], off nt
	global_load_dwordx2 v[48:49], v[72:73], off offset:512 nt
	global_load_dwordx2 v[38:39], v[72:73], off offset:1024 nt
	global_load_dwordx2 v[24:25], v[72:73], off offset:1536 nt
	s_add_i32 s7, s2, s0
	s_cmp_gt_i32 s7, 0xffff
	s_waitcnt vmcnt(24)
	v_mov_b64_e32 v[18:19], v[0:1]
	v_mov_b64_e32 v[16:17], v[2:3]
	s_cbranch_scc1 .LBB0_1395
	s_add_i32 s22, s6, -3
	s_ashr_i32 s23, s22, 31
	s_lshl_b64 s[22:23], s[22:23], 2
	s_add_u32 s24, s10, s22
	s_addc_u32 s25, s11, s23
	s_add_u32 s22, s12, s22
	s_addc_u32 s23, s13, s23
	s_add_i32 s26, s6, -2
	s_ashr_i32 s27, s26, 31
	s_lshl_b64 s[26:27], s[26:27], 2
	s_add_u32 s28, s10, s26
	s_addc_u32 s29, s11, s27
	s_add_u32 s26, s12, s26
	s_addc_u32 s27, s13, s27
	s_add_i32 s30, s6, -1
	s_ashr_i32 s31, s30, 31
	s_lshl_b64 s[30:31], s[30:31], 2
	s_add_u32 s34, s10, s30
	s_addc_u32 s35, s11, s31
	s_add_u32 s30, s12, s30
	s_addc_u32 s31, s13, s31
	s_ashr_i32 s7, s6, 31
	s_lshl_b64 s[36:37], s[6:7], 2
	s_add_u32 s38, s10, s36
	s_addc_u32 s39, s11, s37
	s_add_u32 s36, s12, s36
	s_addc_u32 s37, s13, s37
	global_load_dword v4, v5, s[24:25] nt
	global_load_dword v18, v5, s[22:23] nt
	global_load_dword v12, v5, s[28:29] nt
	global_load_dword v19, v5, s[26:27] nt
	global_load_dword v14, v5, s[34:35] nt
	global_load_dword v16, v5, s[30:31] nt
	global_load_dword v15, v5, s[38:39] nt
	global_load_dword v17, v5, s[36:37] nt
	s_waitcnt vmcnt(5)
	v_sub_u32_e32 v13, v12, v61
	v_sub_u32_e32 v12, v4, v61
	s_waitcnt vmcnt(3)
	v_sub_u32_e32 v14, v14, v61
	s_waitcnt vmcnt(1)
	v_sub_u32_e32 v15, v15, v61
	s_branch .LBB0_1395
